# speedup vs baseline: 1.0425x; 1.0038x over previous
_Z7k_stageILi0ELi8EEv8AttnArgsPKDF16_PKfPDF16_iii:
	s_load_dwordx16 s[64:79], s[0:1], 0x0
	v_readfirstlane_b32 s94, v0
	s_nop 0
	s_lshr_b32 s94, s94, 6
	s_load_dwordx4 s[8:11], s[0:1], 0x88
	s_lshl_b32 s4, s2, 4
	s_and_b32 s4, s4, 0x70
	s_lshr_b32 s5, s2, 3
	s_add_i32 s4, s4, s5
	s_lshr_b32 s7, s4, 5
	s_lshl_b32 s6, s4, 1
	s_waitcnt lgkmcnt(0)
	s_lshl_b32 s11, s2, 1
	s_cmp_gt_i32 s10, 0
	v_readfirstlane_b32 s24, v0
	s_cbranch_scc1 .LBB3_2
	s_lshl_b32 s31, s7, 12
	s_ashr_i32 s2, s3, 31
	s_mov_b64 s[4:5], 0
	s_branch .LBB3_3

_Z7k_stageILi1ELi4EEv8AttnArgsPKDF16_PKfPDF16_iii:
	s_load_dwordx16 s[64:79], s[0:1], 0x0
	v_readfirstlane_b32 s94, v0
	s_nop 0
	s_lshr_b32 s94, s94, 6
	s_load_dwordx4 s[28:31], s[0:1], 0x70
	s_load_dwordx2 s[24:25], s[0:1], 0x80
	s_load_dword s33, s[0:1], 0x90
	s_lshl_b32 s4, s2, 5
	s_and_b32 s45, s4, 0xe0
	s_lshr_b32 s4, s2, 3
	s_add_i32 s45, s45, s4
	s_and_b32 s44, s2, 56
	v_readfirstlane_b32 s3, v0
	v_and_b32_e32 v1, 15, v0
	s_waitcnt lgkmcnt(0)
	s_cmp_lt_i32 s33, 1
	v_bfe_u32 v167, v0, 4, 2
	s_cbranch_scc1 .LBB4_155
	s_lshr_b32 s2, s3, 2
	v_lshrrev_b32_e32 v7, 7, v0
	v_lshrrev_b32_e32 v2, 5, v0
	v_lshrrev_b32_e32 v3, 4, v0
	s_and_b32 s2, s2, 16
	v_lshrrev_b32_e32 v4, 6, v0
	v_and_b32_e32 v7, 1, v7
	v_and_b32_e32 v2, 4, v2
	v_or_b32_e32 v179, s2, v1
	v_and_b32_e32 v5, 4, v4
	s_load_dwordx2 s[40:41], s[0:1], 0x60
	s_bitcmp1_b32 s3, 6
	v_lshlrev_b16_e32 v7, 2, v7
	v_and_b32_e32 v8, 3, v3
	s_load_dwordx4 s[36:39], s[0:1], 0x0
	s_load_dwordx2 s[4:5], s[0:1], 0x10
	s_load_dwordx8 s[8:15], s[0:1], 0x18
	s_load_dwordx2 s[6:7], s[0:1], 0x38
	s_load_dwordx8 s[16:23], s[0:1], 0x40
	v_or_b32_e32 v178, v2, v167
	v_and_or_b32 v180, s45, 56, v5
	s_cselect_b64 s[26:27], -1, 0
	s_and_b32 s3, s45, 0x3ffffc0
	v_bitop3_b16 v3, v7, v3, 3 bitop3:0xf8
	v_bitop3_b16 v7, v7, 8, v8 bitop3:0xfe
	v_lshlrev_b32_e32 v8, 12, v5
	v_bitop3_b32 v2, v2, v179, v167 bitop3:0x36
	v_or_b32_e32 v6, s3, v180
	s_and_b32 s3, s45, 0x1ffc0
	v_and_b32_e32 v3, 0xffff, v3
	v_lshl_or_b32 v184, v2, 4, v8
	v_lshlrev_b32_e32 v2, 3, v5
	v_mov_b32_e32 v169, 0
	v_lshlrev_b32_e32 v168, 5, v179
	v_lshlrev_b32_e32 v181, 6, v6
	v_or_b32_e32 v6, s3, v180
	v_and_b32_e32 v7, 0xffff, v7
	v_or_b32_e32 v186, 8, v2
	v_or_b32_e32 v188, 16, v2
	v_bitop3_b32 v2, s2, v3, v1 bitop3:0x36
	v_lshlrev_b32_e32 v166, 3, v179
	s_waitcnt lgkmcnt(0)
	v_lshl_add_u64 v[170:171], s[38:39], 0, v[168:169]
	s_mov_b32 s39, 0x20000
	v_lshlrev_b32_e32 v189, 4, v2
	v_bitop3_b32 v2, s2, v7, v1 bitop3:0x36
	v_lshlrev_b32_e32 v193, 15, v6
	v_lshl_add_u64 v[172:173], s[4:5], 0, v[168:169]
	s_and_b32 s37, s37, 0xffff
	s_mov_b32 s38, 0x1800000
	v_add_u32_e32 v182, -1, v180
	v_add_u32_e32 v183, 4, v180
	v_lshl_add_u64 v[174:175], s[14:15], 0, v[168:169]
	v_lshl_add_u64 v[176:177], s[6:7], 0, v[168:169]
	s_and_b32 s13, s13, 0xffff
	s_mov_b32 s42, 0x800000
	s_mov_b32 s43, s39
	s_and_b32 s41, s41, 0xffff
	v_or_b32_e32 v185, 64, v181
	v_or_b32_e32 v187, 0x80, v181
	v_or_b32_e32 v190, 0xc0, v181
	v_lshl_or_b32 v191, v4, 3, 24
	v_lshlrev_b32_e32 v192, 4, v2
	v_lshlrev_b32_e32 v194, 4, v179
	v_or_b32_e32 v195, 0x8000, v193
	v_or_b32_e32 v196, 0x10000, v193
	v_or_b32_e32 v197, 0x18000, v193
	s_mov_b32 s46, 0
	s_movk_i32 s47, 0x300
	v_lshlrev_b32_e32 v198, 1, v166
	s_branch .LBB4_4

_Z7k_stageILi0ELi4EEv8AttnArgsPKDF16_PKfPDF16_iii:
	s_load_dwordx16 s[64:79], s[0:1], 0x0
	v_readfirstlane_b32 s94, v0
	s_nop 0
	s_lshr_b32 s94, s94, 6
	s_load_dwordx4 s[8:11], s[0:1], 0x70
	s_load_dwordx2 s[20:21], s[0:1], 0x80
	s_load_dwordx4 s[12:15], s[0:1], 0x88
	s_lshl_b32 s5, s2, 5
	s_waitcnt lgkmcnt(0)
	s_and_b32 s15, s5, 0xe0
	s_lshr_b32 s5, s2, 3
	s_add_i32 s15, s15, s5
	s_and_b32 s2, s2, 56
	v_readfirstlane_b32 s4, v0
	v_and_b32_e32 v1, 15, v0
	s_cmp_lt_i32 s14, 1
	v_bfe_u32 v158, v0, 4, 2
	s_cbranch_scc1 .LBB5_79
	s_bfe_u32 s5, s4, 0x10006
	s_lshl_b32 s6, s5, 4
	s_mul_i32 s16, s3, 40
	s_mul_hi_i32 s7, s3, 40
	s_add_u32 s22, s0, s16
	s_addc_u32 s23, s1, s7
	s_load_dwordx4 s[16:19], s[22:23], 0x0
	s_load_dwordx2 s[0:1], s[22:23], 0x10
	v_or_b32_e32 v159, s6, v1
	v_lshlrev_b32_e32 v18, 5, v159
	s_waitcnt lgkmcnt(0)
	global_load_dwordx4 v[230:233], v18, s[18:19]
	global_load_dwordx4 v[234:237], v18, s[0:1]
	global_load_dwordx4 v[238:241], v18, s[18:19] offset:16
	global_load_dwordx4 v[242:245], v18, s[0:1] offset:16
	v_bfe_u32 v21, v0, 7, 1
	v_lshrrev_b32_e32 v19, 4, v0
	v_lshlrev_b16_e32 v23, 2, v21
	v_lshrrev_b32_e32 v18, 5, v0
	v_lshrrev_b32_e32 v20, 6, v0
	v_and_b32_e32 v24, 3, v19
	v_bitop3_b16 v19, v23, v19, 3 bitop3:0xf8
	s_movk_i32 s0, 0x3000
	v_and_b32_e32 v18, 4, v18
	v_and_b32_e32 v22, 4, v20
	v_lshlrev_b32_e32 v20, 12, v20
	v_lshlrev_b32_e32 v21, 11, v21
	v_and_b32_e32 v19, 0xffff, v19
	s_bitcmp1_b32 s4, 6
	v_or_b32_e32 v161, v18, v158
	v_and_or_b32 v162, s15, 56, v22
	v_bitop3_b16 v23, v23, 8, v24 bitop3:0xfe
	v_lshlrev_b32_e32 v24, 3, v22
	v_lshl_or_b32 v22, v22, 12, v21
	v_or3_b32 v163, v20, v21, s0
	v_bitop3_b32 v18, v18, v159, v158 bitop3:0x36
	v_bitop3_b32 v19, s6, v19, v1 bitop3:0x36
	s_cselect_b64 s[24:25], -1, 0
	s_and_b32 s0, s15, 0x1ffc0
	s_movk_i32 s1, 0x2000
	v_lshl_or_b32 v168, v18, 4, v22
	v_lshlrev_b32_e32 v18, 4, v19
	v_or_b32_e32 v19, s0, v162
	v_add3_u32 v170, v22, v18, s1
	v_lshl_or_b32 v18, v19, 6, s2
	v_add_u32_e32 v18, v161, v18
	v_mul_u32_u24_e32 v18, 0x600, v18
	v_and_b32_e32 v20, 0xffff, v23
	v_lshl_or_b32 v18, s5, 8, v18
	v_lshlrev_b32_e32 v160, 9, v158
	v_bitop3_b32 v20, s6, v20, v1 bitop3:0x36
	v_lshl_or_b32 v18, v1, 4, v18
	v_add_u32_e32 v164, -1, v162
	v_add_u32_e32 v165, 4, v162
	v_or3_b32 v166, v161, v24, 8
	v_or_b32_e32 v167, 0x1000, v22
	v_lshl_or_b32 v169, v20, 4, v160
	s_and_b32 s17, s17, 0xffff
	s_mov_b32 s19, 0x20000
	s_mov_b32 s18, 0x1800000
	v_add_u32_e32 v171, 0xfffe7c00, v18
	s_mov_b32 s30, s2
	s_mov_b32 s93, 0
	s_branch .LBB5_4
